# P0 entry LayerNorm prefetches the next row while the current one is reduced and stored
# speedup vs baseline: 1.0009x; 1.0009x over previous
; template <int MAP>
; __device__ __forceinline__ void ln_finish(float (&v)[32], const float* __restrict__ g, const float* __restrict__ b, float* xout, bf16* xbout, int lane, bf16* xlout = nullptr, unsigned char* x8out = nullptr, unsigned char* xi8out = nullptr, float* sxout = nullptr) {
;     ...
;             for (int j = 0; j < 8; ++j) { const int c = 4 * (lane + 64 * j); const f32x4 gv = *(const f32x4*)(g + c), bv = *(const f32x4*)(b + c);
;                 v[4 * j] = v[4 * j] * rstd * gv.x + bv.x; v[4 * j + 1] = v[4 * j + 1] * rstd * gv.y + bv.y; v[4 * j + 2] = v[4 * j + 2] * rstd * gv.z + bv.z; v[4 * j + 3] = v[4 * j + 3] * rstd * gv.w + bv.w; }
; __device__ __forceinline__ void entry_ln_row(const Params& p, int t, int lane) {
;     ...
;     float v[32]; const float* xr = p.in[0] + (size_t)t * D;
; #pragma unroll
;     for (int j = 0; j < 8; ++j) { const f32x4 a = __builtin_nontemporal_load((const f32x4*)(xr + 4 * (lane + 64 * j))); v[4 * j] = a.x; v[4 * j + 1] = a.y; v[4 * j + 2] = a.z; v[4 * j + 3] = a.w; }
;     ln_finish<0>(v, p.in[1], p.in[2], nullptr, XB + (size_t)t * D, lane, nullptr, p.ws + WS_X8IN + (size_t)t * D, p.ws + WS_XI8 + (size_t)t * D, (float*)(p.ws + WS_SX) + t);
.LBB0_82:
	s_cmpk_gt_i32 s60, 0x1fff
	v_lshlrev_b32_e32 v66, 4, v130
	s_cbranch_scc1 .LBB0_87
	v_or_b32_e32 v38, 0x1000, v66
	v_or_b32_e32 v46, 0x1400, v66
	v_or_b32_e32 v54, 0x1800, v66
	v_or_b32_e32 v62, 0x1c00, v66
	global_load_dwordx4 v[2:5], v66, s[8:9]
	global_load_dwordx4 v[6:9], v66, s[6:7]
	s_waitcnt lgkmcnt(0)
	global_load_dwordx4 v[10:13], v66, s[8:9] offset:1024
	global_load_dwordx4 v[14:17], v66, s[6:7] offset:1024
	global_load_dwordx4 v[18:21], v66, s[8:9] offset:2048
	global_load_dwordx4 v[22:25], v66, s[6:7] offset:2048
	global_load_dwordx4 v[26:29], v66, s[8:9] offset:3072
	global_load_dwordx4 v[30:33], v66, s[6:7] offset:3072
	global_load_dwordx4 v[34:37], v38, s[8:9]
	s_nop 0
	global_load_dwordx4 v[38:41], v38, s[6:7]
	s_nop 0
	global_load_dwordx4 v[42:45], v46, s[8:9]
	s_nop 0
	global_load_dwordx4 v[46:49], v46, s[6:7]
	s_nop 0
	global_load_dwordx4 v[50:53], v54, s[8:9]
	s_nop 0
	global_load_dwordx4 v[54:57], v54, s[6:7]
	s_nop 0
	global_load_dwordx4 v[58:61], v62, s[8:9]
	s_nop 0
	global_load_dwordx4 v[62:65], v62, s[6:7]
	s_ashr_i32 s3, s63, 31
	s_ashr_i32 s6, s31, 31
	s_add_u32 s2, s63, s31
	s_addc_u32 s3, s3, s6
	s_lshl_b64 s[6:7], s[2:3], 2
	s_add_u32 s38, s6, 0x1b800000
	s_addc_u32 s39, s7, 0
	s_ashr_i32 s31, s30, 31
	s_lshl_b64 s[8:9], s[2:3], 11
	s_lshl_b64 s[6:7], s[30:31], 2
	s_lshl_b64 s[18:19], s[2:3], 13
	v_mov_b32_e32 v67, 0
	v_xor_b32_e32 v110, 4, v135
	v_xor_b32_e32 v111, 8, v135
	v_xor_b32_e32 v112, 16, v135
	v_xor_b32_e32 v113, 32, v135
	v_xor_b32_e32 v114, 64, v135
	v_xor_b32_e32 v115, 0x80, v135
	v_cmp_eq_u32_e64 s[0:1], 0, v130
	v_mov_b32_e32 v116, 0x3727c5ac
	v_mov_b32_e32 v117, 0x260
	s_mov_b32 s40, 0x1e3ce508
	s_mov_b32 s41, 0x42fe0000
	s_mov_b32 s42, 0x40c0c00
	s_mov_b32 s43, 0x1a800000
	s_movk_i32 s44, 0x7fff
	s_mov_b32 s45, 0xc3e00000
	s_mov_b32 s46, 0x19800000
	v_mov_b32_e32 v118, 1
	v_mov_b32_e32 v119, 0x43e00000
	s_mov_b32 s47, s60
	s_waitcnt vmcnt(15)
	v_mov_b32_e32 v68, v3
	v_mov_b32_e32 v69, v5
	v_mov_b32_e32 v3, v4
	s_waitcnt vmcnt(13)
	v_mov_b32_e32 v4, v11
	v_mov_b32_e32 v5, v13
	v_mov_b32_e32 v11, v12
	s_waitcnt vmcnt(11)
	v_mov_b32_e32 v12, v19
	v_mov_b32_e32 v13, v21
	v_mov_b32_e32 v19, v20
	s_waitcnt vmcnt(9)
	v_mov_b32_e32 v20, v27
	v_mov_b32_e32 v21, v29
	v_mov_b32_e32 v27, v28
	s_waitcnt vmcnt(7)
	v_mov_b32_e32 v28, v35
	v_mov_b32_e32 v29, v37
	v_mov_b32_e32 v35, v36
	s_waitcnt vmcnt(5)
	v_mov_b32_e32 v36, v43
	v_mov_b32_e32 v37, v45
	v_mov_b32_e32 v43, v44
	s_waitcnt vmcnt(3)
	v_mov_b32_e32 v44, v51
	v_mov_b32_e32 v45, v53
	v_mov_b32_e32 v51, v52
	s_waitcnt vmcnt(1)
	v_mov_b32_e32 v52, v59
	v_mov_b32_e32 v53, v61
	v_mov_b32_e32 v59, v60
	v_or_b32_e32 v60, s8, v135
	v_mov_b32_e32 v61, s9
	s_lshl_b64 s[8:9], s[30:31], 11
	s_add_u32 s4, s4, s18
	s_addc_u32 s5, s5, s19
	s_lshl_b64 s[2:3], s[2:3], 12
	v_mov_b32_e32 v70, v7
	v_mov_b32_e32 v71, v9
	v_mov_b32_e32 v7, v8
	v_mov_b32_e32 v8, v15
	v_mov_b32_e32 v9, v17
	v_mov_b32_e32 v15, v16
	v_mov_b32_e32 v16, v23
	v_mov_b32_e32 v17, v25
	v_mov_b32_e32 v23, v24
	v_mov_b32_e32 v24, v31
	v_mov_b32_e32 v25, v33
	v_mov_b32_e32 v31, v32
	v_mov_b32_e32 v32, v39
	v_mov_b32_e32 v33, v41
	v_mov_b32_e32 v39, v40
	v_mov_b32_e32 v40, v47
	v_mov_b32_e32 v41, v49
	v_mov_b32_e32 v47, v48
	v_mov_b32_e32 v48, v55
	v_mov_b32_e32 v49, v57
	v_mov_b32_e32 v55, v56
	s_waitcnt vmcnt(0)
	v_mov_b32_e32 v56, v63
	v_mov_b32_e32 v57, v65
	v_mov_b32_e32 v63, v64
	v_lshl_add_u64 v[64:65], s[4:5], 0, v[66:67]
	s_mov_b64 s[4:5], 0x1000
	v_lshl_or_b32 v72, v130, 3, s2
	v_mov_b32_e32 v73, s3
	s_mov_b64 s[2:3], 0x4800800
	v_lshl_add_u64 v[64:65], v[64:65], 0, s[4:5]
	s_lshl_b64 s[4:5], s[30:31], 13
	v_lshl_add_u64 v[72:73], v[72:73], 0, s[2:3]
	s_lshl_b64 s[18:19], s[30:31], 12
	s_mov_b32 s31, 0xf800000
	global_load_dwordx4 v[180:183], v[64:65], off offset:-4096 nt
	global_load_dwordx4 v[184:187], v[64:65], off offset:-3072 nt
	global_load_dwordx4 v[188:191], v[64:65], off offset:-2048 nt
	global_load_dwordx4 v[192:195], v[64:65], off offset:-1024 nt
	global_load_dwordx4 v[196:199], v[64:65], off nt
	global_load_dwordx4 v[200:203], v[64:65], off offset:1024 nt
	global_load_dwordx4 v[204:207], v[64:65], off offset:2048 nt
	global_load_dwordx4 v[208:211], v[64:65], off offset:3072 nt
	s_waitcnt vmcnt(0)
	s_branch .Lmy_ln_top

; template <int MAP>
; __device__ __forceinline__ void ln_finish(float (&v)[32], const float* __restrict__ g, const float* __restrict__ b, float* xout, bf16* xbout, int lane, bf16* xlout = nullptr, unsigned char* x8out = nullptr, unsigned char* xi8out = nullptr, float* sxout = nullptr) {
;     float s = 0.f;
; #pragma unroll
;     for (int i = 0; i < 32; ++i) s += v[i];
;     const float mean = wave_sum(s, lane) * (1.0f / D);
;     float q = 0.f;
; #pragma unroll
;     for (int i = 0; i < 32; ++i) { v[i] -= mean; q += v[i] * v[i]; }
; __device__ __forceinline__ void entry_ln_row(const Params& p, int t, int lane) {
;     ...
;     float v[32]; const float* xr = p.in[0] + (size_t)t * D;
; #pragma unroll
;     for (int j = 0; j < 8; ++j) { const f32x4 a = __builtin_nontemporal_load((const f32x4*)(xr + 4 * (lane + 64 * j))); v[4 * j] = a.x; v[4 * j + 1] = a.y; v[4 * j + 2] = a.z; v[4 * j + 3] = a.w; }
.LBB0_85:
	s_waitcnt vmcnt(24)
.Lmy_ln_top:
	v_mov_b64_e32 v[74:75], v[180:181]
	v_mov_b64_e32 v[76:77], v[182:183]
	v_mov_b64_e32 v[78:79], v[184:185]
	v_mov_b64_e32 v[80:81], v[186:187]
	v_mov_b64_e32 v[82:83], v[188:189]
	v_mov_b64_e32 v[84:85], v[190:191]
	v_mov_b64_e32 v[86:87], v[192:193]
	v_mov_b64_e32 v[88:89], v[194:195]
	v_mov_b64_e32 v[90:91], v[196:197]
	v_mov_b64_e32 v[92:93], v[198:199]
	v_mov_b64_e32 v[94:95], v[200:201]
	v_mov_b64_e32 v[96:97], v[202:203]
	v_mov_b64_e32 v[98:99], v[204:205]
	v_mov_b64_e32 v[100:101], v[206:207]
	v_mov_b64_e32 v[102:103], v[208:209]
	v_mov_b64_e32 v[104:105], v[210:211]
	s_add_i32 vcc_lo, s47, s30
	s_cmpk_gt_i32 vcc_lo, 0x1fff
	s_cbranch_scc1 .Lmy_ln_nopf
	v_lshl_add_u64 v[212:213], v[64:65], 0, s[4:5]
	global_load_dwordx4 v[180:183], v[212:213], off offset:-4096 nt
	global_load_dwordx4 v[184:187], v[212:213], off offset:-3072 nt
	global_load_dwordx4 v[188:191], v[212:213], off offset:-2048 nt
	global_load_dwordx4 v[192:195], v[212:213], off offset:-1024 nt
	global_load_dwordx4 v[196:199], v[212:213], off nt
	global_load_dwordx4 v[200:203], v[212:213], off offset:1024 nt
	global_load_dwordx4 v[204:207], v[212:213], off offset:2048 nt
	global_load_dwordx4 v[208:211], v[212:213], off offset:3072 nt
.Lmy_ln_nopf:
	v_add_f32_e32 v106, 0, v74
	v_add_f32_e32 v106, v75, v106
	v_add_f32_e32 v106, v76, v106
	v_add_f32_e32 v106, v77, v106
	v_add_f32_e32 v106, v78, v106
	v_add_f32_e32 v106, v79, v106
	v_add_f32_e32 v106, v80, v106
	v_add_f32_e32 v106, v81, v106
	v_add_f32_e32 v106, v82, v106
	v_add_f32_e32 v106, v83, v106
	v_add_f32_e32 v106, v84, v106
	v_add_f32_e32 v106, v85, v106
	v_add_f32_e32 v106, v86, v106
	v_add_f32_e32 v106, v87, v106
	v_add_f32_e32 v106, v88, v106
	v_add_f32_e32 v106, v89, v106
	v_add_f32_e32 v106, v90, v106
	v_add_f32_e32 v106, v91, v106
	v_add_f32_e32 v106, v92, v106
	v_add_f32_e32 v106, v93, v106
	v_add_f32_e32 v106, v94, v106
	v_add_f32_e32 v106, v95, v106
	v_add_f32_e32 v106, v96, v106
	v_add_f32_e32 v106, v97, v106
	v_add_f32_e32 v106, v98, v106
	v_add_f32_e32 v106, v99, v106
	v_add_f32_e32 v106, v100, v106
	v_add_f32_e32 v106, v101, v106
	v_add_f32_e32 v106, v102, v106
	v_add_f32_e32 v106, v103, v106
	v_add_f32_e32 v106, v104, v106
	v_add_f32_e32 v120, v105, v106
	ds_bpermute_b32 v121, v110, v120
	v_mov_b32_e32 v106, v74
	v_mov_b32_e32 v107, v76
	v_mov_b32_e32 v108, v78
	v_mov_b32_e32 v109, v80
	s_waitcnt lgkmcnt(0)
	v_add_f32_e32 v74, v120, v121
	ds_bpermute_b32 v76, v111, v74
	v_mov_b32_e32 v120, v82
	v_mov_b32_e32 v121, v84
	v_mov_b32_e32 v122, v86
	v_mov_b32_e32 v123, v88
	s_waitcnt lgkmcnt(0)
	v_add_f32_e32 v74, v74, v76
	ds_bpermute_b32 v76, v112, v74
	v_mov_b32_e32 v124, v90
	v_mov_b32_e32 v125, v92
	v_mov_b32_e32 v126, v94
	v_mov_b32_e32 v127, v96
	s_waitcnt lgkmcnt(0)
	v_add_f32_e32 v74, v74, v76
	ds_bpermute_b32 v76, v113, v74
	v_mov_b32_e32 v128, v98
	v_mov_b32_e32 v129, v100
	v_mov_b32_e32 v132, v102
	v_mov_b32_e32 v133, v104
	s_waitcnt lgkmcnt(0)
	v_add_f32_e32 v74, v74, v76
	ds_bpermute_b32 v78, v114, v74
	v_mov_b32_e32 v76, v75
	v_mov_b32_e32 v80, v79
	v_mov_b32_e32 v84, v83
	v_mov_b32_e32 v88, v87
	s_waitcnt lgkmcnt(0)
	v_add_f32_e32 v74, v74, v78
	ds_bpermute_b32 v75, v115, v74
	v_mov_b32_e32 v92, v91
	v_mov_b32_e32 v96, v95
	v_mov_b32_e32 v100, v99
	v_mov_b32_e32 v104, v103
	s_waitcnt lgkmcnt(0)
	v_add_f32_e32 v74, v74, v75
	v_mul_f32_e32 v74, 0x3a000000, v74
	v_pk_add_f32 v[78:79], v[106:107], v[74:75] op_sel_hi:[1,0] neg_lo:[0,1] neg_hi:[0,1]
	v_pk_add_f32 v[76:77], v[76:77], v[74:75] op_sel_hi:[1,0] neg_lo:[0,1] neg_hi:[0,1]
	v_pk_add_f32 v[82:83], v[108:109], v[74:75] op_sel_hi:[1,0] neg_lo:[0,1] neg_hi:[0,1]
	v_pk_add_f32 v[80:81], v[80:81], v[74:75] op_sel_hi:[1,0] neg_lo:[0,1] neg_hi:[0,1]
	v_pk_add_f32 v[86:87], v[120:121], v[74:75] op_sel_hi:[1,0] neg_lo:[0,1] neg_hi:[0,1]
	v_pk_add_f32 v[84:85], v[84:85], v[74:75] op_sel_hi:[1,0] neg_lo:[0,1] neg_hi:[0,1]
	v_pk_add_f32 v[90:91], v[122:123], v[74:75] op_sel_hi:[1,0] neg_lo:[0,1] neg_hi:[0,1]
	v_pk_add_f32 v[88:89], v[88:89], v[74:75] op_sel_hi:[1,0] neg_lo:[0,1] neg_hi:[0,1]
	v_pk_add_f32 v[94:95], v[124:125], v[74:75] op_sel_hi:[1,0] neg_lo:[0,1] neg_hi:[0,1]
	v_pk_add_f32 v[92:93], v[92:93], v[74:75] op_sel_hi:[1,0] neg_lo:[0,1] neg_hi:[0,1]
	v_pk_add_f32 v[98:99], v[126:127], v[74:75] op_sel_hi:[1,0] neg_lo:[0,1] neg_hi:[0,1]
	v_pk_add_f32 v[96:97], v[96:97], v[74:75] op_sel_hi:[1,0] neg_lo:[0,1] neg_hi:[0,1]
	v_pk_add_f32 v[102:103], v[128:129], v[74:75] op_sel_hi:[1,0] neg_lo:[0,1] neg_hi:[0,1]
	v_pk_add_f32 v[100:101], v[100:101], v[74:75] op_sel_hi:[1,0] neg_lo:[0,1] neg_hi:[0,1]
	v_pk_add_f32 v[106:107], v[132:133], v[74:75] op_sel_hi:[1,0] neg_lo:[0,1] neg_hi:[0,1]
	v_pk_add_f32 v[74:75], v[104:105], v[74:75] op_sel_hi:[1,0] neg_lo:[0,1] neg_hi:[0,1]
	v_pk_mul_f32 v[104:105], v[78:79], v[78:79]
	v_pk_mul_f32 v[108:109], v[76:77], v[76:77]
	v_pk_mul_f32 v[120:121], v[82:83], v[82:83]
	v_add_f32_e32 v104, v104, v108
	v_add_f32_e32 v104, v105, v104
	v_add_f32_e32 v104, v109, v104
	v_pk_mul_f32 v[122:123], v[80:81], v[80:81]
	v_add_f32_e32 v104, v120, v104
	v_add_f32_e32 v104, v122, v104
	v_add_f32_e32 v104, v121, v104
	v_pk_mul_f32 v[124:125], v[86:87], v[86:87]
	v_add_f32_e32 v104, v123, v104
	v_pk_mul_f32 v[126:127], v[84:85], v[84:85]
	v_add_f32_e32 v104, v124, v104
	v_add_f32_e32 v104, v126, v104
	v_add_f32_e32 v104, v125, v104
	v_pk_mul_f32 v[128:129], v[90:91], v[90:91]
	v_add_f32_e32 v104, v127, v104
	v_pk_mul_f32 v[132:133], v[88:89], v[88:89]
	v_add_f32_e32 v104, v128, v104
	v_add_f32_e32 v104, v132, v104
	v_add_f32_e32 v104, v129, v104
	v_pk_mul_f32 v[138:139], v[94:95], v[94:95]
	v_add_f32_e32 v104, v133, v104
	v_pk_mul_f32 v[140:141], v[92:93], v[92:93]
	v_add_f32_e32 v104, v138, v104
	v_add_f32_e32 v104, v140, v104
	v_add_f32_e32 v104, v139, v104
	v_pk_mul_f32 v[142:143], v[98:99], v[98:99]
	v_add_f32_e32 v104, v141, v104
	v_pk_mul_f32 v[144:145], v[96:97], v[96:97]
	v_add_f32_e32 v104, v142, v104
	v_add_f32_e32 v104, v144, v104
	v_add_f32_e32 v104, v143, v104
	v_pk_mul_f32 v[146:147], v[102:103], v[102:103]
	v_add_f32_e32 v104, v145, v104
	v_pk_mul_f32 v[148:149], v[100:101], v[100:101]
	v_add_f32_e32 v104, v146, v104
	v_add_f32_e32 v104, v148, v104
	v_add_f32_e32 v104, v147, v104
	v_add_f32_e32 v104, v149, v104
	v_mov_b32_e32 v150, v75
	v_mov_b32_e32 v151, v107
	v_fmac_f32_e32 v104, v106, v106
	v_pk_mul_f32 v[150:151], v[150:151], v[150:151]
	v_fmac_f32_e32 v104, v74, v74
	v_add_f32_e32 v104, v151, v104
	v_add_f32_e32 v104, v150, v104
	ds_bpermute_b32 v105, v110, v104
	s_waitcnt lgkmcnt(0)
; __device__ __forceinline__ float shx(float v, int mask, int lane) { return __int_as_float(__builtin_amdgcn_ds_bpermute((lane ^ mask) << 2, __float_as_int(v))); }
; template <int MAP>
; __device__ __forceinline__ void ln_finish(float (&v)[32], const float* __restrict__ g, const float* __restrict__ b, float* xout, bf16* xbout, int lane, bf16* xlout = nullptr, unsigned char* x8out = nullptr, unsigned char* xi8out = nullptr, float* sxout = nullptr) {
;     ...
;     const float mean = wave_sum(s, lane) * (1.0f / D);
;     float q = 0.f;
; #pragma unroll
;     for (int i = 0; i < 32; ++i) { v[i] -= mean; q += v[i] * v[i]; }
;     const float rstd = 1.0f / sqrtf(wave_sum(q, lane) * (1.0f / D) + LN_EPS);
;     const bool two = (xi8out != nullptr);
;     float qm = 0.f;
;     if (two) {
;         float am = 0.f;
;         if (MAP == 0) {
; #pragma unroll
;             for (int j = 0; j < 8; ++j) { const int c = 4 * (lane + 64 * j); const f32x4 gv = *(const f32x4*)(g + c), bv = *(const f32x4*)(b + c);
;                 v[4 * j] = v[4 * j] * rstd * gv.x + bv.x; v[4 * j + 1] = v[4 * j + 1] * rstd * gv.y + bv.y; v[4 * j + 2] = v[4 * j + 2] * rstd * gv.z + bv.z; v[4 * j + 3] = v[4 * j + 3] * rstd * gv.w + bv.w; }
;         } else {
; #pragma unroll
;             for (int j = 0; j < 4; ++j) { const int c = 8 * (lane + 64 * j); const f32x4 g0 = *(const f32x4*)(g + c), g1 = *(const f32x4*)(g + c + 4), b0 = *(const f32x4*)(b + c), b1 = *(const f32x4*)(b + c + 4);
;                 v[8 * j] = v[8 * j] * rstd * g0.x + b0.x; v[8 * j + 1] = v[8 * j + 1] * rstd * g0.y + b0.y; v[8 * j + 2] = v[8 * j + 2] * rstd * g0.z + b0.z; v[8 * j + 3] = v[8 * j + 3] * rstd * g0.w + b0.w;
;                 v[8 * j + 4] = v[8 * j + 4] * rstd * g1.x + b1.x; v[8 * j + 5] = v[8 * j + 5] * rstd * g1.y + b1.y; v[8 * j + 6] = v[8 * j + 6] * rstd * g1.z + b1.z; v[8 * j + 7] = v[8 * j + 7] * rstd * g1.w + b1.w; }
;         }
; #pragma unroll
;         for (int i = 0; i < 32; ++i) am = fmaxf(am, fabsf(v[i]));
; #pragma unroll
;         for (int o = 1; o < 64; o <<= 1) am = fmaxf(am, shx(am, o, lane));
;         am = fmaxf(am, 1e-20f); qm = 127.0f / am;
;         if (lane == 0) *sxout = am * (1.0f / 127.0f);
	v_add_f32_e32 v104, v104, v105
	ds_bpermute_b32 v105, v111, v104
	s_waitcnt lgkmcnt(0)
	v_add_f32_e32 v104, v104, v105
	ds_bpermute_b32 v105, v112, v104
	s_waitcnt lgkmcnt(0)
	v_add_f32_e32 v104, v104, v105
	ds_bpermute_b32 v105, v113, v104
	s_waitcnt lgkmcnt(0)
	v_add_f32_e32 v104, v104, v105
	ds_bpermute_b32 v105, v114, v104
	s_waitcnt lgkmcnt(0)
	v_add_f32_e32 v104, v104, v105
	ds_bpermute_b32 v105, v115, v104
	s_waitcnt lgkmcnt(0)
	v_add_f32_e32 v104, v104, v105
	v_fmamk_f32 v104, v104, 0x3a000000, v116
	v_mul_f32_e32 v105, 0x4f800000, v104
	v_cmp_gt_f32_e32 vcc, s31, v104
	s_nop 1
	v_cndmask_b32_e32 v104, v104, v105, vcc
	v_sqrt_f32_e32 v105, v104
	s_nop 0
	v_add_u32_e32 v108, -1, v105
	v_add_u32_e32 v109, 1, v105
	v_fma_f32 v120, -v108, v105, v104
	v_fma_f32 v121, -v109, v105, v104
	v_cmp_ge_f32_e64 s[2:3], 0, v120
	s_nop 1
	v_cndmask_b32_e64 v105, v105, v108, s[2:3]
	v_cmp_lt_f32_e64 s[2:3], 0, v121
	s_nop 1
	v_cndmask_b32_e64 v105, v105, v109, s[2:3]
	v_mul_f32_e32 v108, 0x37800000, v105
	v_cndmask_b32_e32 v105, v105, v108, vcc
	v_cmp_class_f32_e32 vcc, v104, v117
	s_nop 1
	v_cndmask_b32_e32 v104, v105, v104, vcc
	v_div_scale_f32 v105, s[2:3], v104, v104, 1.0
	v_rcp_f32_e32 v108, v105
	v_div_scale_f32 v109, vcc, 1.0, v104, 1.0
	v_fma_f32 v120, -v105, v108, 1.0
	v_fmac_f32_e32 v108, v120, v108
	v_mul_f32_e32 v120, v109, v108
	v_fma_f32 v121, -v105, v120, v109
	v_fmac_f32_e32 v120, v121, v108
	v_fma_f32 v105, -v105, v120, v109
	v_div_fmas_f32 v105, v105, v108, v120
	v_div_fixup_f32 v104, v105, v104, 1.0
	v_pk_mul_f32 v[78:79], v[78:79], v[104:105] op_sel_hi:[1,0]
	v_pk_mul_f32 v[76:77], v[76:77], v[104:105] op_sel_hi:[1,0]
	v_pk_mul_f32 v[86:87], v[86:87], v[104:105] op_sel_hi:[1,0]
	v_pk_mul_f32 v[120:121], v[90:91], v[104:105] op_sel_hi:[1,0]
	v_pk_fma_f32 v[90:91], v[6:7], v[78:79], v[2:3]
	v_pk_fma_f32 v[108:109], v[70:71], v[76:77], v[68:69]
	v_pk_mul_f32 v[82:83], v[82:83], v[104:105] op_sel_hi:[1,0]
	v_pk_mul_f32 v[80:81], v[80:81], v[104:105] op_sel_hi:[1,0]
	v_pk_mul_f32 v[132:133], v[100:101], v[104:105] op_sel_hi:[1,0]
	v_pk_fma_f32 v[100:101], v[22:23], v[86:87], v[18:19]
	v_max3_f32 v86, |v90|, 0, |v108|
	v_pk_mul_f32 v[84:85], v[84:85], v[104:105] op_sel_hi:[1,0]
	v_pk_mul_f32 v[88:89], v[88:89], v[104:105] op_sel_hi:[1,0]
	v_pk_mul_f32 v[94:95], v[94:95], v[104:105] op_sel_hi:[1,0]
	v_pk_mul_f32 v[122:123], v[92:93], v[104:105] op_sel_hi:[1,0]
	v_pk_mul_f32 v[124:125], v[98:99], v[104:105] op_sel_hi:[1,0]
	v_pk_mul_f32 v[126:127], v[96:97], v[104:105] op_sel_hi:[1,0]
	v_pk_mul_f32 v[128:129], v[102:103], v[104:105] op_sel_hi:[1,0]
	v_pk_mul_f32 v[138:139], v[106:107], v[104:105] op_sel_hi:[1,0]
	v_pk_mul_f32 v[140:141], v[74:75], v[104:105] op_sel_hi:[1,0]
	v_pk_fma_f32 v[104:105], v[14:15], v[82:83], v[10:11]
	v_pk_fma_f32 v[106:107], v[8:9], v[80:81], v[4:5]
	v_max3_f32 v86, v86, |v91|, |v109|
	v_max3_f32 v86, v86, |v104|, |v106|
	v_pk_fma_f32 v[102:103], v[16:17], v[84:85], v[12:13]
	v_max3_f32 v86, v86, |v105|, |v107|
	v_max3_f32 v86, v86, |v100|, |v102|
	v_pk_fma_f32 v[96:97], v[30:31], v[120:121], v[26:27]
	v_pk_fma_f32 v[98:99], v[24:25], v[88:89], v[20:21]
	v_max3_f32 v86, v86, |v101|, |v103|
	v_max3_f32 v86, v86, |v96|, |v98|
	v_pk_fma_f32 v[92:93], v[38:39], v[94:95], v[34:35]
	v_pk_fma_f32 v[94:95], v[32:33], v[122:123], v[28:29]
	v_max3_f32 v86, v86, |v97|, |v99|
	v_max3_f32 v86, v86, |v92|, |v94|
	v_pk_fma_f32 v[82:83], v[46:47], v[124:125], v[42:43]
	v_pk_fma_f32 v[84:85], v[40:41], v[126:127], v[36:37]
	v_max3_f32 v86, v86, |v93|, |v95|
	v_max3_f32 v86, v86, |v82|, |v84|
	v_pk_fma_f32 v[78:79], v[54:55], v[128:129], v[50:51]
	v_pk_fma_f32 v[80:81], v[48:49], v[132:133], v[44:45]
	v_max3_f32 v86, v86, |v83|, |v85|
	v_max3_f32 v86, v86, |v78|, |v80|
	v_pk_fma_f32 v[74:75], v[62:63], v[138:139], v[58:59]
	v_pk_fma_f32 v[76:77], v[56:57], v[140:141], v[52:53]
	v_max3_f32 v86, v86, |v79|, |v81|
	v_max3_f32 v86, v86, |v74|, |v76|
	v_max3_f32 v86, v86, |v75|, |v77|
	ds_bpermute_b32 v87, v110, v86
	s_waitcnt lgkmcnt(0)
	v_max_f32_e32 v87, v87, v87
	v_max_f32_e32 v86, v86, v87
	ds_bpermute_b32 v87, v111, v86
	s_waitcnt lgkmcnt(0)
	v_max_f32_e32 v87, v87, v87
	v_max_f32_e32 v86, v86, v87
	ds_bpermute_b32 v87, v112, v86
	s_waitcnt lgkmcnt(0)
	v_max_f32_e32 v87, v87, v87
	v_max_f32_e32 v86, v86, v87
	ds_bpermute_b32 v87, v113, v86
	s_waitcnt lgkmcnt(0)
	v_max_f32_e32 v87, v87, v87
	v_max_f32_e32 v86, v86, v87
	ds_bpermute_b32 v87, v114, v86
	s_waitcnt lgkmcnt(0)
	v_max_f32_e32 v87, v87, v87
	v_max_f32_e32 v86, v86, v87
	ds_bpermute_b32 v87, v115, v86
	s_waitcnt lgkmcnt(0)
	v_max3_f32 v86, v86, v87, s40
	s_and_saveexec_b64 s[2:3], s[0:1]
	s_cbranch_execz .LBB0_84
	s_add_u32 s48, s28, s38
	s_addc_u32 s49, s29, s39
	v_mul_f32_e32 v87, 0x3c010204, v86
	global_store_dword v67, v87, s[48:49]
	s_branch .LBB0_84
